# P0 W1/W2: the 8 waves of a WG take the 8 k-blocks of one column block (WG writes whole 1 KiB dst rows together, in lockstep)
# baseline (speedup 1.0000x reference)
.LBB0_111:
	s_mov_b32 s4, 20
	s_waitcnt vmcnt(2)
	v_mov_b32_e32 v10, v0
	s_nop 0
	v_readfirstlane_b32 s5, v10
	s_ashr_i32 s6, s5, 6
	s_add_i32 s8, s6, s3
	s_cmp_gt_i32 s8, 0xffff
	s_cbranch_scc1 .LBB0_116
	s_ashr_i32 s5, s4, 31
	s_lshl_b64 s[4:5], s[4:5], 3
	s_add_u32 s4, s94, s4
	s_addc_u32 s5, s95, s5
	s_lshl_b32 s6, s6, 14
	s_add_i32 s9, s6, 0
	s_mov_b32 s100, s8
	s_and_b32 s101, s100, 7
	s_lshl_b32 s101, s101, 6
	s_bfe_u32 s8, s100, 0x30006
	s_or_b32 s8, s8, s101
	s_andn2_b32 s101, s100, 0x1c7
	s_or_b32 s8, s8, s101
	s_ashr_i32 s6, s8, 31
	s_load_dwordx2 s[4:5], s[4:5], 0x0
	s_lshr_b32 s6, s6, 23
	s_add_i32 s10, s8, s6
	s_ashr_i32 s6, s10, 9
	s_ashr_i32 s7, s6, 31
	s_lshl_b64 s[6:7], s[6:7], 23
	s_waitcnt lgkmcnt(0)
	s_add_u32 s11, s4, s6
	s_addc_u32 s12, s5, s7
	s_and_b32 s6, s10, 0xfffffe00
	s_sub_i32 s6, s8, s6
	s_mov_b32 s8, s100
	s_ashr_i32 s7, s6, 31
	s_lshr_b32 s7, s7, 26
	s_add_i32 s7, s6, s7
	s_and_b32 s10, s7, 0x7ffffc0
	s_sub_i32 s6, s6, s10
	s_lshl_b32 s7, s7, 1
	s_and_b32 s7, s7, 0xffffff80
	s_lshl_b32 s6, s6, 5
	v_bfe_u32 v1, v10, 3, 3
	s_waitcnt vmcnt(0)
	v_or_b32_e32 v2, s7, v1
	s_ashr_i32 s7, s6, 31
	s_lshl_b64 s[6:7], s[6:7], 2
	v_lshlrev_b32_e32 v3, 2, v10
	s_add_u32 s6, s11, s6
	v_and_b32_e32 v12, 28, v3
	s_addc_u32 s7, s12, s7
	v_mov_b32_e32 v137, 0
	v_lshlrev_b32_e32 v136, 2, v12
	v_ashrrev_i32_e32 v3, 31, v2
	v_or_b32_e32 v8, 8, v2
	v_lshl_add_u64 v[4:5], s[6:7], 0, v[136:137]
	v_lshlrev_b64 v[6:7], 13, v[2:3]
	v_ashrrev_i32_e32 v9, 31, v8
	v_lshl_add_u64 v[6:7], v[4:5], 0, v[6:7]
	v_lshlrev_b64 v[8:9], 13, v[8:9]
	v_lshl_add_u64 v[8:9], v[4:5], 0, v[8:9]
	global_load_dwordx4 v[126:129], v[6:7], off nt
	global_load_dwordx4 v[122:125], v[8:9], off nt
	v_or_b32_e32 v6, 16, v2
	v_ashrrev_i32_e32 v7, 31, v6
	v_or_b32_e32 v8, 24, v2
	v_lshlrev_b64 v[6:7], 13, v[6:7]
	v_ashrrev_i32_e32 v9, 31, v8
	v_lshl_add_u64 v[6:7], v[4:5], 0, v[6:7]
	v_lshlrev_b64 v[8:9], 13, v[8:9]
	v_lshl_add_u64 v[8:9], v[4:5], 0, v[8:9]
	global_load_dwordx4 v[118:121], v[6:7], off nt
	global_load_dwordx4 v[114:117], v[8:9], off nt
	v_or_b32_e32 v6, 32, v2
	v_ashrrev_i32_e32 v7, 31, v6
	v_or_b32_e32 v8, 40, v2
	v_lshlrev_b64 v[6:7], 13, v[6:7]
	v_ashrrev_i32_e32 v9, 31, v8
	v_lshl_add_u64 v[6:7], v[4:5], 0, v[6:7]
	v_lshlrev_b64 v[8:9], 13, v[8:9]
	v_lshl_add_u64 v[8:9], v[4:5], 0, v[8:9]
	global_load_dwordx4 v[110:113], v[6:7], off nt
	global_load_dwordx4 v[106:109], v[8:9], off nt
	v_or_b32_e32 v6, 48, v2
	v_ashrrev_i32_e32 v7, 31, v6
	v_or_b32_e32 v8, 56, v2
	v_lshlrev_b64 v[6:7], 13, v[6:7]
	v_ashrrev_i32_e32 v9, 31, v8
	v_lshl_add_u64 v[6:7], v[4:5], 0, v[6:7]
	v_lshlrev_b64 v[8:9], 13, v[8:9]
	v_lshl_add_u64 v[8:9], v[4:5], 0, v[8:9]
	global_load_dwordx4 v[94:97], v[6:7], off nt
	global_load_dwordx4 v[82:85], v[8:9], off nt
	v_or_b32_e32 v6, 64, v2
	v_ashrrev_i32_e32 v7, 31, v6
	v_or_b32_e32 v8, 0x48, v2
	v_lshlrev_b64 v[6:7], 13, v[6:7]
	v_ashrrev_i32_e32 v9, 31, v8
	v_lshl_add_u64 v[6:7], v[4:5], 0, v[6:7]
	v_lshlrev_b64 v[8:9], 13, v[8:9]
	v_lshl_add_u64 v[8:9], v[4:5], 0, v[8:9]
	global_load_dwordx4 v[70:73], v[6:7], off nt
	global_load_dwordx4 v[58:61], v[8:9], off nt
	v_or_b32_e32 v6, 0x50, v2
	v_ashrrev_i32_e32 v7, 31, v6
	v_or_b32_e32 v8, 0x58, v2
	v_lshlrev_b64 v[6:7], 13, v[6:7]
	v_ashrrev_i32_e32 v9, 31, v8
	v_lshl_add_u64 v[6:7], v[4:5], 0, v[6:7]
	v_lshlrev_b64 v[8:9], 13, v[8:9]
	v_lshl_add_u64 v[8:9], v[4:5], 0, v[8:9]
	global_load_dwordx4 v[54:57], v[6:7], off nt
	global_load_dwordx4 v[34:37], v[8:9], off nt
	v_or_b32_e32 v6, 0x60, v2
	v_ashrrev_i32_e32 v7, 31, v6
	v_or_b32_e32 v8, 0x68, v2
	v_lshlrev_b64 v[6:7], 13, v[6:7]
	v_ashrrev_i32_e32 v9, 31, v8
	v_lshl_add_u64 v[6:7], v[4:5], 0, v[6:7]
	v_lshlrev_b64 v[8:9], 13, v[8:9]
	v_lshl_add_u64 v[8:9], v[4:5], 0, v[8:9]
	global_load_dwordx4 v[30:33], v[6:7], off nt
	global_load_dwordx4 v[18:21], v[8:9], off nt
	v_or_b32_e32 v6, 0x70, v2
	v_ashrrev_i32_e32 v7, 31, v6
	v_or_b32_e32 v2, 0x78, v2
	v_lshlrev_b64 v[6:7], 13, v[6:7]
	v_ashrrev_i32_e32 v3, 31, v2
	v_lshl_add_u64 v[14:15], v[4:5], 0, v[6:7]
	v_lshlrev_b64 v[2:3], 13, v[2:3]
	v_lshl_add_u64 v[16:17], v[4:5], 0, v[2:3]
	global_load_dwordx4 v[6:9], v[14:15], off nt
	global_load_dwordx4 v[2:5], v[16:17], off nt
	v_and_b32_e32 v10, 63, v10
	v_lshlrev_b32_e32 v10, 4, v10
	v_mul_u32_u24_e32 v11, 0x90, v12
	v_and_b32_e32 v140, 0x70, v10
	s_mov_b64 s[6:7], 0x18000000
	v_add3_u32 v144, s9, v11, v1
	v_add_u32_e32 v11, s9, v140
	v_mul_u32_u24_e32 v13, 0x90, v1
	v_lshl_add_u64 v[138:139], v[132:133], 0, s[6:7]
	v_mov_b32_e32 v141, v137
	v_and_b32_e32 v145, 0x80, v10
	v_or_b32_e32 v146, 8, v1
	v_or_b32_e32 v147, 16, v1
	v_or_b32_e32 v148, 24, v1
	v_lshlrev_b32_e32 v136, 2, v12
	v_add_u32_e32 v149, v11, v13
	s_branch .LBB0_114
.LBB0_113:
	s_waitcnt vmcnt(15)
	v_mul_f32_e32 v126, 0x42800000, v126
	v_mul_f32_e32 v127, 0x42800000, v127
	v_mov_b32_e32 v150, 0
	v_cvt_pk_fp8_f32 v150, v126, v127
	v_mul_f32_e32 v126, 0x42800000, v128
	v_mul_f32_e32 v127, 0x42800000, v129
	s_waitcnt vmcnt(14)
	v_mul_f32_e32 v122, 0x42800000, v122
	v_cvt_pk_fp8_f32 v150, v126, v127 op_sel:[0,0,1]
	v_mul_f32_e32 v123, 0x42800000, v123
	v_mov_b32_e32 v127, 0
	v_cvt_pk_fp8_f32 v127, v122, v123
	v_mul_f32_e32 v122, 0x42800000, v124
	v_mul_f32_e32 v123, 0x42800000, v125
	s_waitcnt vmcnt(13)
	v_mul_f32_e32 v118, 0x42800000, v118
	v_cvt_pk_fp8_f32 v127, v122, v123 op_sel:[0,0,1]
	v_mul_f32_e32 v119, 0x42800000, v119
	v_mov_b32_e32 v123, 0
	v_cvt_pk_fp8_f32 v123, v118, v119
	v_mul_f32_e32 v118, 0x42800000, v120
	v_mul_f32_e32 v119, 0x42800000, v121
	s_waitcnt vmcnt(12)
	v_mul_f32_e32 v114, 0x42800000, v114
	v_cvt_pk_fp8_f32 v123, v118, v119 op_sel:[0,0,1]
	v_mul_f32_e32 v115, 0x42800000, v115
	v_mov_b32_e32 v119, 0
	v_cvt_pk_fp8_f32 v119, v114, v115
	v_mul_f32_e32 v114, 0x42800000, v116
	v_mul_f32_e32 v115, 0x42800000, v117
	s_waitcnt vmcnt(11)
	v_mul_f32_e32 v110, 0x42800000, v110
	v_cvt_pk_fp8_f32 v119, v114, v115 op_sel:[0,0,1]
	v_mul_f32_e32 v111, 0x42800000, v111
	v_mov_b32_e32 v115, 0
	v_cvt_pk_fp8_f32 v115, v110, v111
	v_mul_f32_e32 v110, 0x42800000, v112
	v_mul_f32_e32 v111, 0x42800000, v113
	s_waitcnt vmcnt(10)
	v_mul_f32_e32 v106, 0x42800000, v106
	v_cvt_pk_fp8_f32 v115, v110, v111 op_sel:[0,0,1]
	v_mul_f32_e32 v107, 0x42800000, v107
	v_mov_b32_e32 v111, 0
	v_cvt_pk_fp8_f32 v111, v106, v107
	v_mul_f32_e32 v106, 0x42800000, v108
	v_mul_f32_e32 v107, 0x42800000, v109
	s_waitcnt vmcnt(9)
	v_mul_f32_e32 v94, 0x42800000, v94
	v_cvt_pk_fp8_f32 v111, v106, v107 op_sel:[0,0,1]
	v_mul_f32_e32 v95, 0x42800000, v95
	v_mov_b32_e32 v107, 0
	v_cvt_pk_fp8_f32 v107, v94, v95
	v_mul_f32_e32 v94, 0x42800000, v96
	v_mul_f32_e32 v95, 0x42800000, v97
	s_waitcnt vmcnt(8)
	v_mul_f32_e32 v82, 0x42800000, v82
	v_cvt_pk_fp8_f32 v107, v94, v95 op_sel:[0,0,1]
	v_mul_f32_e32 v83, 0x42800000, v83
	v_mov_b32_e32 v95, 0
	v_cvt_pk_fp8_f32 v95, v82, v83
	v_mul_f32_e32 v82, 0x42800000, v84
	v_mul_f32_e32 v83, 0x42800000, v85
	s_waitcnt vmcnt(7)
	v_mul_f32_e32 v70, 0x42800000, v70
	v_cvt_pk_fp8_f32 v95, v82, v83 op_sel:[0,0,1]
	v_mul_f32_e32 v71, 0x42800000, v71
	v_mov_b32_e32 v83, 0
	v_cvt_pk_fp8_f32 v83, v70, v71
	v_mul_f32_e32 v70, 0x42800000, v72
	v_mul_f32_e32 v71, 0x42800000, v73
	s_waitcnt vmcnt(6)
	v_mul_f32_e32 v58, 0x42800000, v58
	v_cvt_pk_fp8_f32 v83, v70, v71 op_sel:[0,0,1]
	v_mul_f32_e32 v59, 0x42800000, v59
	v_mov_b32_e32 v71, 0
	v_cvt_pk_fp8_f32 v71, v58, v59
	v_mul_f32_e32 v58, 0x42800000, v60
	v_mul_f32_e32 v59, 0x42800000, v61
	s_waitcnt vmcnt(5)
	v_mul_f32_e32 v54, 0x42800000, v54
	v_cvt_pk_fp8_f32 v71, v58, v59 op_sel:[0,0,1]
	v_mul_f32_e32 v55, 0x42800000, v55
	v_mov_b32_e32 v59, 0
	v_cvt_pk_fp8_f32 v59, v54, v55
	v_mul_f32_e32 v54, 0x42800000, v56
	v_mul_f32_e32 v55, 0x42800000, v57
	s_waitcnt vmcnt(4)
	v_mul_f32_e32 v34, 0x42800000, v34
	v_cvt_pk_fp8_f32 v59, v54, v55 op_sel:[0,0,1]
	v_mul_f32_e32 v35, 0x42800000, v35
	v_mov_b32_e32 v55, 0
	v_cvt_pk_fp8_f32 v55, v34, v35
	v_mul_f32_e32 v34, 0x42800000, v36
	v_mul_f32_e32 v35, 0x42800000, v37
	s_waitcnt vmcnt(3)
	v_mul_f32_e32 v30, 0x42800000, v30
	v_cvt_pk_fp8_f32 v55, v34, v35 op_sel:[0,0,1]
	v_mul_f32_e32 v31, 0x42800000, v31
	v_mov_b32_e32 v35, 0
	v_cvt_pk_fp8_f32 v35, v30, v31
	v_mul_f32_e32 v30, 0x42800000, v32
	v_mul_f32_e32 v31, 0x42800000, v33
	s_waitcnt vmcnt(2)
	v_mul_f32_e32 v18, 0x42800000, v18
	v_cvt_pk_fp8_f32 v35, v30, v31 op_sel:[0,0,1]
	v_mul_f32_e32 v19, 0x42800000, v19
	v_mov_b32_e32 v31, 0
	v_cvt_pk_fp8_f32 v31, v18, v19
	v_lshrrev_b32_e32 v126, 8, v150
	v_lshrrev_b32_e32 v122, 24, v150
	v_mul_f32_e32 v18, 0x42800000, v20
	v_mul_f32_e32 v19, 0x42800000, v21
	ds_write_b8 v144, v150
	ds_write_b8 v144, v126 offset:144
	ds_write_b8_d16_hi v144, v150 offset:288
	ds_write_b8 v144, v122 offset:432
	ds_write_b8 v144, v127 offset:8
	v_lshrrev_b32_e32 v122, 8, v127
	v_lshrrev_b32_e32 v118, 24, v127
	v_cvt_pk_fp8_f32 v31, v18, v19 op_sel:[0,0,1]
	s_waitcnt vmcnt(1)
	v_mul_f32_e32 v6, 0x42800000, v6
	v_mul_f32_e32 v7, 0x42800000, v7
	v_mov_b32_e32 v19, 0
	ds_write_b8 v144, v122 offset:152
	ds_write_b8_d16_hi v144, v127 offset:296
	ds_write_b8 v144, v118 offset:440
	ds_write_b8 v144, v123 offset:16
	v_lshrrev_b32_e32 v118, 8, v123
	v_lshrrev_b32_e32 v114, 24, v123
	v_cvt_pk_fp8_f32 v19, v6, v7
	ds_write_b8 v144, v118 offset:160
	ds_write_b8_d16_hi v144, v123 offset:304
	ds_write_b8 v144, v114 offset:448
	ds_write_b8 v144, v119 offset:24
	v_lshrrev_b32_e32 v114, 8, v119
	v_lshrrev_b32_e32 v110, 24, v119
	ds_write_b8 v144, v114 offset:168
	ds_write_b8_d16_hi v144, v119 offset:312
	ds_write_b8 v144, v110 offset:456
	ds_write_b8 v144, v115 offset:32
	v_lshrrev_b32_e32 v110, 8, v115
	v_lshrrev_b32_e32 v106, 24, v115
	ds_write_b8 v144, v110 offset:176
	ds_write_b8_d16_hi v144, v115 offset:320
	ds_write_b8 v144, v106 offset:464
	ds_write_b8 v144, v111 offset:40
	v_lshrrev_b32_e32 v106, 8, v111
	v_lshrrev_b32_e32 v94, 24, v111
	v_mul_f32_e32 v6, 0x42800000, v8
	v_mul_f32_e32 v7, 0x42800000, v9
	ds_write_b8 v144, v106 offset:184
	ds_write_b8_d16_hi v144, v111 offset:328
	ds_write_b8 v144, v94 offset:472
	ds_write_b8 v144, v107 offset:48
	v_lshrrev_b32_e32 v94, 8, v107
	v_lshrrev_b32_e32 v82, 24, v107
	v_cvt_pk_fp8_f32 v19, v6, v7 op_sel:[0,0,1]
	s_waitcnt vmcnt(0)
	v_mul_f32_e32 v2, 0x42800000, v2
	v_mul_f32_e32 v3, 0x42800000, v3
	v_mov_b32_e32 v7, 0
	s_mov_b32 s100, s8
	s_and_b32 s101, s100, 7
	s_lshl_b32 s101, s101, 6
	s_bfe_u32 s8, s100, 0x30006
	s_or_b32 s8, s8, s101
	s_andn2_b32 s101, s100, 0x1c7
	s_or_b32 s8, s8, s101
	s_ashr_i32 s9, s8, 31
	ds_write_b8 v144, v94 offset:192
	ds_write_b8_d16_hi v144, v107 offset:336
	ds_write_b8 v144, v82 offset:480
	ds_write_b8 v144, v95 offset:56
	v_lshrrev_b32_e32 v82, 8, v95
	v_lshrrev_b32_e32 v70, 24, v95
	v_cvt_pk_fp8_f32 v7, v2, v3
	s_lshr_b32 s9, s9, 23
	ds_write_b8 v144, v82 offset:200
	ds_write_b8_d16_hi v144, v95 offset:344
	ds_write_b8 v144, v70 offset:488
	ds_write_b8 v144, v83 offset:64
	v_lshrrev_b32_e32 v70, 8, v83
	v_lshrrev_b32_e32 v58, 24, v83
	s_add_i32 s9, s8, s9
	ds_write_b8 v144, v70 offset:208
	ds_write_b8_d16_hi v144, v83 offset:352
	ds_write_b8 v144, v58 offset:496
	ds_write_b8 v144, v71 offset:72
	v_lshrrev_b32_e32 v58, 8, v71
	v_lshrrev_b32_e32 v54, 24, v71
	s_ashr_i32 s12, s9, 9
	s_and_b32 s9, s9, 0xfffffe00
	ds_write_b8 v144, v58 offset:216
	ds_write_b8_d16_hi v144, v71 offset:360
	ds_write_b8 v144, v54 offset:504
	ds_write_b8 v144, v59 offset:80
	v_lshrrev_b32_e32 v54, 8, v59
	v_lshrrev_b32_e32 v34, 24, v59
	v_mul_f32_e32 v2, 0x42800000, v4
	v_mul_f32_e32 v3, 0x42800000, v5
	s_sub_i32 s9, s8, s9
	ds_write_b8 v144, v54 offset:224
	ds_write_b8_d16_hi v144, v59 offset:368
	ds_write_b8 v144, v34 offset:512
	ds_write_b8 v144, v55 offset:88
	v_lshrrev_b32_e32 v34, 8, v55
	v_lshrrev_b32_e32 v30, 24, v55
	v_cvt_pk_fp8_f32 v7, v2, v3 op_sel:[0,0,1]
	s_ashr_i32 s8, s9, 31
	ds_write_b8 v144, v34 offset:232
	ds_write_b8_d16_hi v144, v55 offset:376
	ds_write_b8 v144, v30 offset:520
	ds_write_b8 v144, v35 offset:96
	v_lshrrev_b32_e32 v30, 8, v35
	v_lshrrev_b32_e32 v18, 24, v35
	s_lshr_b32 s8, s8, 26
	ds_write_b8 v144, v30 offset:240
	ds_write_b8_d16_hi v144, v35 offset:384
	ds_write_b8 v144, v18 offset:528
	ds_write_b8 v144, v31 offset:104
	v_lshrrev_b32_e32 v18, 8, v31
	v_lshrrev_b32_e32 v6, 24, v31
	s_add_i32 s11, s9, s8
	ds_write_b8 v144, v18 offset:248
	ds_write_b8_d16_hi v144, v31 offset:392
	ds_write_b8 v144, v6 offset:536
	ds_write_b8 v144, v19 offset:112
	v_lshrrev_b32_e32 v6, 8, v19
	v_lshrrev_b32_e32 v2, 24, v19
	s_lshl_b32 s8, s11, 1
	ds_write_b8 v144, v6 offset:256
	ds_write_b8_d16_hi v144, v19 offset:400
	ds_write_b8 v144, v2 offset:544
	ds_write_b8 v144, v7 offset:120
	v_lshrrev_b32_e32 v2, 8, v7
	s_and_b32 s11, s11, 0x7ffffc0
	s_ashr_i32 s13, s12, 31
	ds_write_b8 v144, v2 offset:264
	ds_write_b8_d16_hi v144, v7 offset:408
	v_lshrrev_b32_e32 v2, 24, v7
	s_sub_i32 s9, s9, s11
	s_lshl_b64 s[12:13], s[12:13], 21
	s_and_b32 s8, s8, 0xffffff80
	ds_write_b8 v144, v2 offset:552
	s_lshl_b32 s11, s9, 5
	v_lshl_add_u64 v[142:143], v[138:139], 0, s[12:13]
	s_waitcnt lgkmcnt(0)
	s_ashr_i32 s9, s8, 31
	v_or_b32_e32 v6, s11, v1
	v_lshl_add_u64 v[2:3], v[142:143], 0, s[8:9]
	v_lshrrev_b32_e32 v6, 1, v6
	s_and_b32 s12, s11, 0xffffff00
	v_lshl_add_u64 v[18:19], v[2:3], 0, v[140:141]
	ds_read_b128 v[2:5], v149
	v_and_b32_e32 v6, 0x73, v6
	v_or3_b32 v6, v145, v6, s12
	v_ashrrev_i32_e32 v7, 31, v6
	v_lshlrev_b64 v[6:7], 10, v[6:7]
	v_lshl_add_u64 v[20:21], v[18:19], 0, v[6:7]
	ds_read_b128 v[6:9], v149 offset:1152
	s_waitcnt lgkmcnt(1)
	global_store_dwordx4 v[20:21], v[2:5], off nt
	v_mov_b64_e32 v[30:31], v[90:91]
	v_mov_b64_e32 v[34:35], v[74:75]
	v_or_b32_e32 v2, s11, v146
	v_lshrrev_b32_e32 v2, 1, v2
	v_and_b32_e32 v2, 0x77, v2
	v_or3_b32 v2, v145, v2, s12
	v_ashrrev_i32_e32 v3, 31, v2
	v_lshlrev_b64 v[2:3], 10, v[2:3]
	v_lshl_add_u64 v[2:3], v[18:19], 0, v[2:3]
	s_waitcnt lgkmcnt(0)
	global_store_dwordx4 v[2:3], v[6:9], off nt
	ds_read_b128 v[2:5], v149 offset:2304
	v_mov_b64_e32 v[54:55], v[78:79]
	v_or_b32_e32 v6, s11, v147
	v_lshrrev_b32_e32 v6, 1, v6
	v_and_b32_e32 v6, 0x7b, v6
	v_or3_b32 v6, v145, v6, s12
	v_ashrrev_i32_e32 v7, 31, v6
	v_lshlrev_b64 v[6:7], 10, v[6:7]
	v_lshl_add_u64 v[20:21], v[18:19], 0, v[6:7]
	ds_read_b128 v[6:9], v149 offset:3456
	s_waitcnt lgkmcnt(1)
	global_store_dwordx4 v[20:21], v[2:5], off nt
	v_mov_b64_e32 v[58:59], v[62:63]
	v_mov_b64_e32 v[72:73], v[68:69]
	v_or_b32_e32 v2, s11, v148
	v_bfe_u32 v2, v2, 1, 7
	v_or3_b32 v2, v145, v2, s12
	v_ashrrev_i32_e32 v3, 31, v2
	v_lshlrev_b64 v[2:3], 10, v[2:3]
	v_lshl_add_u64 v[2:3], v[18:19], 0, v[2:3]
	s_waitcnt lgkmcnt(0)
	global_store_dwordx4 v[2:3], v[6:9], off nt
	s_waitcnt lgkmcnt(0)
	v_mov_b64_e32 v[2:3], v[98:99]
	v_mov_b64_e32 v[18:19], v[86:87]
	v_mov_b64_e32 v[6:7], v[102:103]
	v_mov_b64_e32 v[84:85], v[48:49]
	v_mov_b64_e32 v[96:97], v[52:53]
	v_mov_b64_e32 v[108:109], v[40:41]
	v_mov_b64_e32 v[112:113], v[44:45]
	v_mov_b64_e32 v[116:117], v[24:25]
	v_mov_b64_e32 v[120:121], v[28:29]
	v_mov_b64_e32 v[124:125], v[12:13]
	v_mov_b64_e32 v[128:129], v[16:17]
	s_andn2_b64 vcc, exec, s[6:7]
	v_mov_b64_e32 v[4:5], v[100:101]
	v_mov_b64_e32 v[8:9], v[104:105]
	v_mov_b64_e32 v[20:21], v[88:89]
	v_mov_b64_e32 v[32:33], v[92:93]
	v_mov_b64_e32 v[36:37], v[76:77]
	v_mov_b64_e32 v[56:57], v[80:81]
	v_mov_b64_e32 v[60:61], v[64:65]
	v_mov_b64_e32 v[70:71], v[66:67]
	v_mov_b64_e32 v[82:83], v[46:47]
	v_mov_b64_e32 v[94:95], v[50:51]
	v_mov_b64_e32 v[106:107], v[38:39]
	v_mov_b64_e32 v[110:111], v[42:43]
	v_mov_b64_e32 v[114:115], v[22:23]
	v_mov_b64_e32 v[118:119], v[26:27]
	v_mov_b64_e32 v[122:123], v[10:11]
	v_mov_b64_e32 v[126:127], v[14:15]
	s_mov_b32 s8, s10
	s_cbranch_vccz .LBB0_116
.LBB0_114:
	s_barrier
	s_add_i32 s10, s8, s2
	s_cmp_gt_i32 s10, 0xffff
	s_cselect_b64 s[6:7], -1, 0
	s_and_b64 vcc, exec, s[6:7]
	s_cbranch_vccnz .LBB0_113
	s_mov_b32 s100, s10
	s_and_b32 s101, s100, 7
	s_lshl_b32 s101, s101, 6
	s_bfe_u32 s10, s100, 0x30006
	s_or_b32 s10, s10, s101
	s_andn2_b32 s101, s100, 0x1c7
	s_or_b32 s10, s10, s101
	s_ashr_i32 s9, s10, 31
	s_lshr_b32 s9, s9, 23
	s_add_i32 s9, s10, s9
	s_ashr_i32 s12, s9, 9
	s_ashr_i32 s13, s12, 31
	s_lshl_b64 s[12:13], s[12:13], 23
	s_add_u32 s11, s4, s12
	s_addc_u32 s14, s5, s13
	s_and_b32 s9, s9, 0xfffffe00
	s_sub_i32 s9, s10, s9
	s_mov_b32 s10, s100
	s_ashr_i32 s12, s9, 31
	s_lshr_b32 s12, s12, 26
	s_add_i32 s12, s9, s12
	s_and_b32 s13, s12, 0x7ffffc0
	s_sub_i32 s9, s9, s13
	s_lshl_b32 s12, s12, 1
	s_and_b32 s13, s12, 0xffffff80
	s_lshl_b32 s12, s9, 5
	v_or_b32_e32 v98, s13, v1
	s_ashr_i32 s13, s12, 31
	s_lshl_b64 s[12:13], s[12:13], 2
	s_add_u32 s12, s11, s12
	s_addc_u32 s13, s14, s13
	v_ashrrev_i32_e32 v99, 31, v98
	v_lshl_add_u64 v[100:101], s[12:13], 0, v[136:137]
	v_lshlrev_b64 v[10:11], 13, v[98:99]
	v_lshl_add_u64 v[22:23], v[100:101], 0, v[10:11]
	v_or_b32_e32 v10, 8, v98
	v_ashrrev_i32_e32 v11, 31, v10
	v_lshlrev_b64 v[10:11], 13, v[10:11]
	v_lshl_add_u64 v[24:25], v[100:101], 0, v[10:11]
	global_load_dwordx4 v[14:17], v[22:23], off nt
	global_load_dwordx4 v[10:13], v[24:25], off nt
	v_or_b32_e32 v22, 16, v98
	v_ashrrev_i32_e32 v23, 31, v22
	v_lshlrev_b64 v[22:23], 13, v[22:23]
	v_lshl_add_u64 v[38:39], v[100:101], 0, v[22:23]
	v_or_b32_e32 v22, 24, v98
	v_ashrrev_i32_e32 v23, 31, v22
	v_lshlrev_b64 v[22:23], 13, v[22:23]
	v_lshl_add_u64 v[40:41], v[100:101], 0, v[22:23]
	global_load_dwordx4 v[26:29], v[38:39], off nt
	global_load_dwordx4 v[22:25], v[40:41], off nt
	v_or_b32_e32 v38, 32, v98
	v_ashrrev_i32_e32 v39, 31, v38
	v_lshlrev_b64 v[38:39], 13, v[38:39]
	v_lshl_add_u64 v[46:47], v[100:101], 0, v[38:39]
	v_or_b32_e32 v38, 40, v98
	v_ashrrev_i32_e32 v39, 31, v38
	v_lshlrev_b64 v[38:39], 13, v[38:39]
	v_lshl_add_u64 v[48:49], v[100:101], 0, v[38:39]
	global_load_dwordx4 v[42:45], v[46:47], off nt
	global_load_dwordx4 v[38:41], v[48:49], off nt
	v_or_b32_e32 v46, 48, v98
	v_ashrrev_i32_e32 v47, 31, v46
	v_lshlrev_b64 v[46:47], 13, v[46:47]
	v_lshl_add_u64 v[62:63], v[100:101], 0, v[46:47]
	v_or_b32_e32 v46, 56, v98
	v_ashrrev_i32_e32 v47, 31, v46
	v_lshlrev_b64 v[46:47], 13, v[46:47]
	v_lshl_add_u64 v[64:65], v[100:101], 0, v[46:47]
	global_load_dwordx4 v[50:53], v[62:63], off nt
	global_load_dwordx4 v[46:49], v[64:65], off nt
	v_or_b32_e32 v62, 64, v98
	v_or_b32_e32 v64, 0x48, v98
	v_or_b32_e32 v74, 0x50, v98
	v_or_b32_e32 v76, 0x58, v98
	v_or_b32_e32 v86, 0x60, v98
	v_or_b32_e32 v88, 0x68, v98
	v_or_b32_e32 v102, 0x70, v98
	v_or_b32_e32 v98, 0x78, v98
	v_ashrrev_i32_e32 v63, 31, v62
	v_ashrrev_i32_e32 v65, 31, v64
	v_ashrrev_i32_e32 v75, 31, v74
	v_ashrrev_i32_e32 v77, 31, v76
	v_ashrrev_i32_e32 v87, 31, v86
	v_ashrrev_i32_e32 v89, 31, v88
	v_ashrrev_i32_e32 v103, 31, v102
	v_ashrrev_i32_e32 v99, 31, v98
	v_lshlrev_b64 v[62:63], 13, v[62:63]
	v_lshlrev_b64 v[64:65], 13, v[64:65]
	v_lshlrev_b64 v[74:75], 13, v[74:75]
	v_lshlrev_b64 v[76:77], 13, v[76:77]
	v_lshlrev_b64 v[86:87], 13, v[86:87]
	v_lshlrev_b64 v[88:89], 13, v[88:89]
	v_lshlrev_b64 v[102:103], 13, v[102:103]
	v_lshlrev_b64 v[98:99], 13, v[98:99]
	v_lshl_add_u64 v[62:63], v[100:101], 0, v[62:63]
	v_lshl_add_u64 v[64:65], v[100:101], 0, v[64:65]
	v_lshl_add_u64 v[74:75], v[100:101], 0, v[74:75]
	v_lshl_add_u64 v[76:77], v[100:101], 0, v[76:77]
	v_lshl_add_u64 v[86:87], v[100:101], 0, v[86:87]
	v_lshl_add_u64 v[88:89], v[100:101], 0, v[88:89]
	v_lshl_add_u64 v[102:103], v[100:101], 0, v[102:103]
	v_lshl_add_u64 v[98:99], v[100:101], 0, v[98:99]
	global_load_dwordx4 v[66:69], v[62:63], off nt
	s_nop 0
	global_load_dwordx4 v[62:65], v[64:65], off nt
	s_nop 0
	global_load_dwordx4 v[78:81], v[74:75], off nt
	s_nop 0
	global_load_dwordx4 v[74:77], v[76:77], off nt
	s_nop 0
	global_load_dwordx4 v[90:93], v[86:87], off nt
	s_nop 0
	global_load_dwordx4 v[86:89], v[88:89], off nt
	s_nop 0
	global_load_dwordx4 v[102:105], v[102:103], off nt
	s_nop 0
	global_load_dwordx4 v[98:101], v[98:99], off nt
	s_branch .LBB0_113
.LBB0_116:
	s_mov_b32 s4, 22
	v_mov_b32_e32 v14, v0
	s_nop 0
	v_readfirstlane_b32 s5, v14
	s_ashr_i32 s6, s5, 6
	s_add_i32 s8, s6, s3
	s_cmpk_gt_i32 s8, 0x7fff
	s_cbranch_scc1 .LBB0_121
	s_ashr_i32 s5, s4, 31
	s_lshl_b64 s[4:5], s[4:5], 3
	s_add_u32 s4, s94, s4
	s_addc_u32 s5, s95, s5
	s_lshl_b32 s6, s6, 14
	s_add_i32 s9, s6, 0
	s_mov_b32 s100, s8
	s_and_b32 s101, s100, 7
	s_lshl_b32 s101, s101, 5
	s_bfe_u32 s8, s100, 0x30005
	s_or_b32 s8, s8, s101
	s_andn2_b32 s101, s100, 0xe7
	s_or_b32 s8, s8, s101
	s_ashr_i32 s6, s8, 31
	s_load_dwordx2 s[4:5], s[4:5], 0x0
	s_lshr_b32 s6, s6, 24
	s_add_i32 s10, s8, s6
	s_ashr_i32 s6, s10, 8
	s_ashr_i32 s7, s6, 31
	s_lshl_b64 s[6:7], s[6:7], 22
	s_waitcnt lgkmcnt(0)
	s_add_u32 s11, s4, s6
	s_addc_u32 s12, s5, s7
	s_and_b32 s6, s10, 0xffffff00
	s_sub_i32 s6, s8, s6
	s_mov_b32 s8, s100
	s_ashr_i32 s7, s6, 31
	s_lshr_b32 s7, s7, 27
	s_add_i32 s7, s6, s7
	s_and_b32 s10, s7, 0x7ffffe0
	s_sub_i32 s6, s6, s10
	s_lshl_b32 s7, s7, 2
	s_and_b32 s7, s7, 0xffffff80
	s_lshl_b32 s6, s6, 5
	v_bfe_u32 v1, v14, 3, 3
	s_waitcnt vmcnt(0)
	v_or_b32_e32 v2, s7, v1
	s_ashr_i32 s7, s6, 31
	s_lshl_b64 s[6:7], s[6:7], 2
	v_lshlrev_b32_e32 v3, 2, v14
	s_add_u32 s6, s11, s6
	v_and_b32_e32 v16, 28, v3
	s_addc_u32 s7, s12, s7
	v_mov_b32_e32 v137, 0
	v_lshlrev_b32_e32 v136, 2, v16
	v_ashrrev_i32_e32 v3, 31, v2
	v_or_b32_e32 v8, 8, v2
	v_lshl_add_u64 v[4:5], s[6:7], 0, v[136:137]
	v_lshlrev_b64 v[6:7], 12, v[2:3]
	v_ashrrev_i32_e32 v9, 31, v8
	v_lshl_add_u64 v[6:7], v[4:5], 0, v[6:7]
	v_lshlrev_b64 v[8:9], 12, v[8:9]
	v_lshl_add_u64 v[8:9], v[4:5], 0, v[8:9]
	global_load_dwordx4 v[126:129], v[6:7], off nt
	global_load_dwordx4 v[122:125], v[8:9], off nt
	v_or_b32_e32 v6, 16, v2
	v_ashrrev_i32_e32 v7, 31, v6
	v_or_b32_e32 v8, 24, v2
	v_lshlrev_b64 v[6:7], 12, v[6:7]
	v_ashrrev_i32_e32 v9, 31, v8
	v_lshl_add_u64 v[6:7], v[4:5], 0, v[6:7]
	v_lshlrev_b64 v[8:9], 12, v[8:9]
	v_lshl_add_u64 v[8:9], v[4:5], 0, v[8:9]
	global_load_dwordx4 v[118:121], v[6:7], off nt
	global_load_dwordx4 v[114:117], v[8:9], off nt
	v_or_b32_e32 v6, 32, v2
	v_ashrrev_i32_e32 v7, 31, v6
	v_or_b32_e32 v8, 40, v2
	v_lshlrev_b64 v[6:7], 12, v[6:7]
	v_ashrrev_i32_e32 v9, 31, v8
	v_lshl_add_u64 v[6:7], v[4:5], 0, v[6:7]
	v_lshlrev_b64 v[8:9], 12, v[8:9]
	v_lshl_add_u64 v[8:9], v[4:5], 0, v[8:9]
	global_load_dwordx4 v[110:113], v[6:7], off nt
	global_load_dwordx4 v[98:101], v[8:9], off nt
	v_or_b32_e32 v6, 48, v2
	v_ashrrev_i32_e32 v7, 31, v6
	v_or_b32_e32 v8, 56, v2
	v_lshlrev_b64 v[6:7], 12, v[6:7]
	v_ashrrev_i32_e32 v9, 31, v8
	v_lshl_add_u64 v[6:7], v[4:5], 0, v[6:7]
	v_lshlrev_b64 v[8:9], 12, v[8:9]
	v_lshl_add_u64 v[8:9], v[4:5], 0, v[8:9]
	global_load_dwordx4 v[86:89], v[6:7], off nt
	global_load_dwordx4 v[74:77], v[8:9], off nt
	v_or_b32_e32 v6, 64, v2
	v_ashrrev_i32_e32 v7, 31, v6
	v_or_b32_e32 v8, 0x48, v2
	v_lshlrev_b64 v[6:7], 12, v[6:7]
	v_ashrrev_i32_e32 v9, 31, v8
	v_lshl_add_u64 v[6:7], v[4:5], 0, v[6:7]
	v_lshlrev_b64 v[8:9], 12, v[8:9]
	v_lshl_add_u64 v[8:9], v[4:5], 0, v[8:9]
	global_load_dwordx4 v[70:73], v[6:7], off nt
	global_load_dwordx4 v[50:53], v[8:9], off nt
	v_or_b32_e32 v6, 0x50, v2
	v_ashrrev_i32_e32 v7, 31, v6
	v_or_b32_e32 v8, 0x58, v2
	v_lshlrev_b64 v[6:7], 12, v[6:7]
	v_ashrrev_i32_e32 v9, 31, v8
	v_lshl_add_u64 v[6:7], v[4:5], 0, v[6:7]
	v_lshlrev_b64 v[8:9], 12, v[8:9]
	v_lshl_add_u64 v[8:9], v[4:5], 0, v[8:9]
	global_load_dwordx4 v[46:49], v[6:7], off nt
	global_load_dwordx4 v[34:37], v[8:9], off nt
	v_or_b32_e32 v6, 0x60, v2
	v_ashrrev_i32_e32 v7, 31, v6
	v_or_b32_e32 v8, 0x68, v2
	v_lshlrev_b64 v[6:7], 12, v[6:7]
	v_ashrrev_i32_e32 v9, 31, v8
	v_lshl_add_u64 v[6:7], v[4:5], 0, v[6:7]
	v_lshlrev_b64 v[8:9], 12, v[8:9]
	v_lshl_add_u64 v[8:9], v[4:5], 0, v[8:9]
	global_load_dwordx4 v[22:25], v[6:7], off nt
	global_load_dwordx4 v[10:13], v[8:9], off nt
	v_or_b32_e32 v6, 0x70, v2
	v_ashrrev_i32_e32 v7, 31, v6
	v_or_b32_e32 v2, 0x78, v2
	v_lshlrev_b64 v[6:7], 12, v[6:7]
	v_ashrrev_i32_e32 v3, 31, v2
	v_lshl_add_u64 v[18:19], v[4:5], 0, v[6:7]
	v_lshlrev_b64 v[2:3], 12, v[2:3]
	v_lshl_add_u64 v[20:21], v[4:5], 0, v[2:3]
	global_load_dwordx4 v[6:9], v[18:19], off nt
	global_load_dwordx4 v[2:5], v[20:21], off nt
	v_lshlrev_b32_e32 v14, 4, v14
	v_mul_u32_u24_e32 v15, 0x90, v16
	v_and_b32_e32 v138, 0x70, v14
	s_mov_b64 s[6:7], 0x38000000
	v_add3_u32 v142, s9, v15, v1
	v_add_u32_e32 v14, s9, v138
	v_mul_u32_u24_e32 v15, 0x90, v1
	v_lshl_add_u64 v[132:133], v[132:133], 0, s[6:7]
	v_or_b32_e32 v143, 8, v1
	v_or_b32_e32 v144, 16, v1
	v_or_b32_e32 v145, 24, v1
	v_mov_b32_e32 v139, v137
	v_lshlrev_b32_e32 v136, 2, v16
	v_add_u32_e32 v146, v14, v15
	s_branch .LBB0_119
.LBB0_118:
	s_waitcnt vmcnt(15)
	v_mul_f32_e32 v126, 0x42800000, v126
	v_mul_f32_e32 v127, 0x42800000, v127
	v_mov_b32_e32 v147, 0
	v_cvt_pk_fp8_f32 v147, v126, v127
	v_mul_f32_e32 v126, 0x42800000, v128
	v_mul_f32_e32 v127, 0x42800000, v129
	s_waitcnt vmcnt(14)
	v_mul_f32_e32 v122, 0x42800000, v122
	v_cvt_pk_fp8_f32 v147, v126, v127 op_sel:[0,0,1]
	v_mul_f32_e32 v123, 0x42800000, v123
	v_mov_b32_e32 v127, 0
	v_cvt_pk_fp8_f32 v127, v122, v123
	v_mul_f32_e32 v122, 0x42800000, v124
	v_mul_f32_e32 v123, 0x42800000, v125
	s_waitcnt vmcnt(13)
	v_mul_f32_e32 v118, 0x42800000, v118
	v_cvt_pk_fp8_f32 v127, v122, v123 op_sel:[0,0,1]
	v_mul_f32_e32 v119, 0x42800000, v119
	v_mov_b32_e32 v123, 0
	v_cvt_pk_fp8_f32 v123, v118, v119
	v_mul_f32_e32 v118, 0x42800000, v120
	v_mul_f32_e32 v119, 0x42800000, v121
	s_waitcnt vmcnt(12)
	v_mul_f32_e32 v114, 0x42800000, v114
	v_cvt_pk_fp8_f32 v123, v118, v119 op_sel:[0,0,1]
	v_mul_f32_e32 v115, 0x42800000, v115
	v_mov_b32_e32 v119, 0
	v_cvt_pk_fp8_f32 v119, v114, v115
	v_mul_f32_e32 v114, 0x42800000, v116
	v_mul_f32_e32 v115, 0x42800000, v117
	s_waitcnt vmcnt(11)
	v_mul_f32_e32 v110, 0x42800000, v110
	v_cvt_pk_fp8_f32 v119, v114, v115 op_sel:[0,0,1]
	v_mul_f32_e32 v111, 0x42800000, v111
	v_mov_b32_e32 v115, 0
	v_cvt_pk_fp8_f32 v115, v110, v111
	v_mul_f32_e32 v110, 0x42800000, v112
	v_mul_f32_e32 v111, 0x42800000, v113
	s_waitcnt vmcnt(10)
	v_mul_f32_e32 v98, 0x42800000, v98
	v_cvt_pk_fp8_f32 v115, v110, v111 op_sel:[0,0,1]
	v_mul_f32_e32 v99, 0x42800000, v99
	v_mov_b32_e32 v111, 0
	v_cvt_pk_fp8_f32 v111, v98, v99
	v_mul_f32_e32 v98, 0x42800000, v100
	v_mul_f32_e32 v99, 0x42800000, v101
	s_waitcnt vmcnt(9)
	v_mul_f32_e32 v86, 0x42800000, v86
	v_cvt_pk_fp8_f32 v111, v98, v99 op_sel:[0,0,1]
	v_mul_f32_e32 v87, 0x42800000, v87
	v_mov_b32_e32 v99, 0
	v_cvt_pk_fp8_f32 v99, v86, v87
	v_mul_f32_e32 v86, 0x42800000, v88
	v_mul_f32_e32 v87, 0x42800000, v89
	s_waitcnt vmcnt(8)
	v_mul_f32_e32 v74, 0x42800000, v74
	v_cvt_pk_fp8_f32 v99, v86, v87 op_sel:[0,0,1]
	v_mul_f32_e32 v75, 0x42800000, v75
	v_mov_b32_e32 v87, 0
	v_cvt_pk_fp8_f32 v87, v74, v75
	v_mul_f32_e32 v74, 0x42800000, v76
	v_mul_f32_e32 v75, 0x42800000, v77
	s_waitcnt vmcnt(7)
	v_mul_f32_e32 v70, 0x42800000, v70
	v_cvt_pk_fp8_f32 v87, v74, v75 op_sel:[0,0,1]
	v_mul_f32_e32 v71, 0x42800000, v71
	v_mov_b32_e32 v75, 0
	v_cvt_pk_fp8_f32 v75, v70, v71
	v_mul_f32_e32 v70, 0x42800000, v72
	v_mul_f32_e32 v71, 0x42800000, v73
	s_waitcnt vmcnt(6)
	v_mul_f32_e32 v50, 0x42800000, v50
	v_cvt_pk_fp8_f32 v75, v70, v71 op_sel:[0,0,1]
	v_mul_f32_e32 v51, 0x42800000, v51
	v_mov_b32_e32 v71, 0
	v_cvt_pk_fp8_f32 v71, v50, v51
	v_mul_f32_e32 v50, 0x42800000, v52
	v_mul_f32_e32 v51, 0x42800000, v53
	s_waitcnt vmcnt(5)
	v_mul_f32_e32 v46, 0x42800000, v46
	v_cvt_pk_fp8_f32 v71, v50, v51 op_sel:[0,0,1]
	v_mul_f32_e32 v47, 0x42800000, v47
	v_mov_b32_e32 v51, 0
	v_cvt_pk_fp8_f32 v51, v46, v47
	v_mul_f32_e32 v46, 0x42800000, v48
	v_mul_f32_e32 v47, 0x42800000, v49
	s_waitcnt vmcnt(4)
	v_mul_f32_e32 v34, 0x42800000, v34
	v_cvt_pk_fp8_f32 v51, v46, v47 op_sel:[0,0,1]
	v_mul_f32_e32 v35, 0x42800000, v35
	v_mov_b32_e32 v47, 0
	v_cvt_pk_fp8_f32 v47, v34, v35
	v_mul_f32_e32 v34, 0x42800000, v36
	v_mul_f32_e32 v35, 0x42800000, v37
	s_waitcnt vmcnt(3)
	v_mul_f32_e32 v22, 0x42800000, v22
	v_cvt_pk_fp8_f32 v47, v34, v35 op_sel:[0,0,1]
	v_mul_f32_e32 v23, 0x42800000, v23
	v_mov_b32_e32 v35, 0
	v_cvt_pk_fp8_f32 v35, v22, v23
	v_mul_f32_e32 v22, 0x42800000, v24
	v_mul_f32_e32 v23, 0x42800000, v25
	s_waitcnt vmcnt(2)
	v_mul_f32_e32 v10, 0x42800000, v10
	v_cvt_pk_fp8_f32 v35, v22, v23 op_sel:[0,0,1]
	v_mul_f32_e32 v11, 0x42800000, v11
	v_mov_b32_e32 v23, 0
	v_cvt_pk_fp8_f32 v23, v10, v11
	v_lshrrev_b32_e32 v126, 8, v147
	v_lshrrev_b32_e32 v122, 24, v147
	v_mul_f32_e32 v10, 0x42800000, v12
	v_mul_f32_e32 v11, 0x42800000, v13
	ds_write_b8 v142, v147
	ds_write_b8 v142, v126 offset:144
	ds_write_b8_d16_hi v142, v147 offset:288
	ds_write_b8 v142, v122 offset:432
	ds_write_b8 v142, v127 offset:8
	v_lshrrev_b32_e32 v122, 8, v127
	v_lshrrev_b32_e32 v118, 24, v127
	v_cvt_pk_fp8_f32 v23, v10, v11 op_sel:[0,0,1]
	s_waitcnt vmcnt(1)
	v_mul_f32_e32 v6, 0x42800000, v6
	v_mul_f32_e32 v7, 0x42800000, v7
	v_mov_b32_e32 v11, 0
	ds_write_b8 v142, v122 offset:152
	ds_write_b8_d16_hi v142, v127 offset:296
	ds_write_b8 v142, v118 offset:440
	ds_write_b8 v142, v123 offset:16
	v_lshrrev_b32_e32 v118, 8, v123
	v_lshrrev_b32_e32 v114, 24, v123
	v_cvt_pk_fp8_f32 v11, v6, v7
	ds_write_b8 v142, v118 offset:160
	ds_write_b8_d16_hi v142, v123 offset:304
	ds_write_b8 v142, v114 offset:448
	ds_write_b8 v142, v119 offset:24
	v_lshrrev_b32_e32 v114, 8, v119
	v_lshrrev_b32_e32 v110, 24, v119
	ds_write_b8 v142, v114 offset:168
	ds_write_b8_d16_hi v142, v119 offset:312
	ds_write_b8 v142, v110 offset:456
	ds_write_b8 v142, v115 offset:32
	v_lshrrev_b32_e32 v110, 8, v115
	v_lshrrev_b32_e32 v98, 24, v115
	ds_write_b8 v142, v110 offset:176
	ds_write_b8_d16_hi v142, v115 offset:320
	ds_write_b8 v142, v98 offset:464
	ds_write_b8 v142, v111 offset:40
	v_lshrrev_b32_e32 v98, 8, v111
	v_lshrrev_b32_e32 v86, 24, v111
	v_mul_f32_e32 v6, 0x42800000, v8
	v_mul_f32_e32 v7, 0x42800000, v9
	ds_write_b8 v142, v98 offset:184
	ds_write_b8_d16_hi v142, v111 offset:328
	ds_write_b8 v142, v86 offset:472
	ds_write_b8 v142, v99 offset:48
	v_lshrrev_b32_e32 v86, 8, v99
	v_lshrrev_b32_e32 v74, 24, v99
	v_cvt_pk_fp8_f32 v11, v6, v7 op_sel:[0,0,1]
	s_waitcnt vmcnt(0)
	v_mul_f32_e32 v2, 0x42800000, v2
	v_mul_f32_e32 v3, 0x42800000, v3
	v_mov_b32_e32 v7, 0
	ds_write_b8 v142, v86 offset:192
	ds_write_b8_d16_hi v142, v99 offset:336
	ds_write_b8 v142, v74 offset:480
	ds_write_b8 v142, v87 offset:56
	v_lshrrev_b32_e32 v74, 8, v87
	v_lshrrev_b32_e32 v70, 24, v87
	v_cvt_pk_fp8_f32 v7, v2, v3
	s_mov_b32 s100, s8
	s_and_b32 s101, s100, 7
	s_lshl_b32 s101, s101, 5
	s_bfe_u32 s8, s100, 0x30005
	s_or_b32 s8, s8, s101
	s_andn2_b32 s101, s100, 0xe7
	s_or_b32 s8, s8, s101
	s_ashr_i32 s9, s8, 31
	ds_write_b8 v142, v74 offset:200
	ds_write_b8_d16_hi v142, v87 offset:344
	ds_write_b8 v142, v70 offset:488
	ds_write_b8 v142, v75 offset:64
	v_lshrrev_b32_e32 v70, 8, v75
	v_lshrrev_b32_e32 v50, 24, v75
	s_lshr_b32 s9, s9, 24
	ds_write_b8 v142, v70 offset:208
	ds_write_b8_d16_hi v142, v75 offset:352
	ds_write_b8 v142, v50 offset:496
	ds_write_b8 v142, v71 offset:72
	v_lshrrev_b32_e32 v50, 8, v71
	v_lshrrev_b32_e32 v46, 24, v71
	s_add_i32 s9, s8, s9
	ds_write_b8 v142, v50 offset:216
	ds_write_b8_d16_hi v142, v71 offset:360
	ds_write_b8 v142, v46 offset:504
	ds_write_b8 v142, v51 offset:80
	v_lshrrev_b32_e32 v46, 8, v51
	v_lshrrev_b32_e32 v34, 24, v51
	v_mul_f32_e32 v2, 0x42800000, v4
	v_mul_f32_e32 v3, 0x42800000, v5
	s_ashr_i32 s12, s9, 8
	s_and_b32 s9, s9, 0xffffff00
	ds_write_b8 v142, v46 offset:224
	ds_write_b8_d16_hi v142, v51 offset:368
	ds_write_b8 v142, v34 offset:512
	ds_write_b8 v142, v47 offset:88
	v_lshrrev_b32_e32 v34, 8, v47
	v_lshrrev_b32_e32 v22, 24, v47
	v_cvt_pk_fp8_f32 v7, v2, v3 op_sel:[0,0,1]
	s_sub_i32 s9, s8, s9
	ds_write_b8 v142, v34 offset:232
	ds_write_b8_d16_hi v142, v47 offset:376
	ds_write_b8 v142, v22 offset:520
	ds_write_b8 v142, v35 offset:96
	v_lshrrev_b32_e32 v22, 8, v35
	v_lshrrev_b32_e32 v10, 24, v35
	s_ashr_i32 s8, s9, 31
	ds_write_b8 v142, v22 offset:240
	ds_write_b8_d16_hi v142, v35 offset:384
	ds_write_b8 v142, v10 offset:528
	ds_write_b8 v142, v23 offset:104
	v_lshrrev_b32_e32 v10, 8, v23
	v_lshrrev_b32_e32 v6, 24, v23
	s_lshr_b32 s8, s8, 27
	ds_write_b8 v142, v10 offset:248
	ds_write_b8_d16_hi v142, v23 offset:392
	ds_write_b8 v142, v6 offset:536
	ds_write_b8 v142, v11 offset:112
	v_lshrrev_b32_e32 v6, 8, v11
	v_lshrrev_b32_e32 v2, 24, v11
	s_add_i32 s11, s9, s8
	ds_write_b8 v142, v6 offset:256
	ds_write_b8_d16_hi v142, v11 offset:400
	ds_write_b8 v142, v2 offset:544
	ds_write_b8 v142, v7 offset:120
	v_lshrrev_b32_e32 v2, 8, v7
	s_ashr_i32 s13, s12, 31
	s_lshl_b32 s8, s11, 2
	ds_write_b8 v142, v2 offset:264
	ds_write_b8_d16_hi v142, v7 offset:408
	v_lshrrev_b32_e32 v2, 24, v7
	s_and_b32 s11, s11, 0x7ffffe0
	s_lshl_b64 s[12:13], s[12:13], 20
	s_and_b32 s8, s8, 0xffffff80
	ds_write_b8 v142, v2 offset:552
	s_sub_i32 s9, s9, s11
	v_lshl_add_u64 v[140:141], v[132:133], 0, s[12:13]
	s_lshl_b32 s11, s9, 5
	s_waitcnt lgkmcnt(0)
	s_ashr_i32 s9, s8, 31
	v_lshl_add_u64 v[2:3], v[140:141], 0, s[8:9]
	v_lshl_add_u64 v[10:11], v[2:3], 0, v[138:139]
	ds_read_b128 v[2:5], v146
	v_or_b32_e32 v6, s11, v1
	v_ashrrev_i32_e32 v7, 31, v6
	v_lshlrev_b64 v[6:7], 10, v[6:7]
	v_lshl_add_u64 v[12:13], v[10:11], 0, v[6:7]
	ds_read_b128 v[6:9], v146 offset:1152
	s_waitcnt lgkmcnt(1)
	global_store_dwordx4 v[12:13], v[2:5], off nt
	v_mov_b64_e32 v[22:23], v[94:95]
	v_mov_b64_e32 v[34:35], v[78:79]
	v_or_b32_e32 v2, s11, v143
	v_ashrrev_i32_e32 v3, 31, v2
	v_lshlrev_b64 v[2:3], 10, v[2:3]
	v_lshl_add_u64 v[2:3], v[10:11], 0, v[2:3]
	s_waitcnt lgkmcnt(0)
	global_store_dwordx4 v[2:3], v[6:9], off nt
	ds_read_b128 v[2:5], v146 offset:2304
	v_mov_b64_e32 v[46:47], v[82:83]
	v_or_b32_e32 v6, s11, v144
	v_ashrrev_i32_e32 v7, 31, v6
	v_lshlrev_b64 v[6:7], 10, v[6:7]
	v_lshl_add_u64 v[12:13], v[10:11], 0, v[6:7]
	ds_read_b128 v[6:9], v146 offset:3456
	s_waitcnt lgkmcnt(1)
	global_store_dwordx4 v[12:13], v[2:5], off nt
	v_mov_b64_e32 v[50:51], v[62:63]
	v_mov_b64_e32 v[72:73], v[68:69]
	v_or_b32_e32 v2, s11, v145
	v_ashrrev_i32_e32 v3, 31, v2
	v_lshlrev_b64 v[2:3], 10, v[2:3]
	v_lshl_add_u64 v[2:3], v[10:11], 0, v[2:3]
	s_waitcnt lgkmcnt(0)
	global_store_dwordx4 v[2:3], v[6:9], off nt
	s_waitcnt lgkmcnt(0)
	v_mov_b64_e32 v[2:3], v[102:103]
	v_mov_b64_e32 v[10:11], v[90:91]
	v_mov_b64_e32 v[6:7], v[106:107]
	v_mov_b64_e32 v[76:77], v[56:57]
	v_mov_b64_e32 v[88:89], v[60:61]
	v_mov_b64_e32 v[100:101], v[40:41]
	v_mov_b64_e32 v[112:113], v[44:45]
	v_mov_b64_e32 v[116:117], v[28:29]
	v_mov_b64_e32 v[120:121], v[32:33]
	v_mov_b64_e32 v[124:125], v[16:17]
	v_mov_b64_e32 v[128:129], v[20:21]
	s_andn2_b64 vcc, exec, s[6:7]
	v_mov_b64_e32 v[4:5], v[104:105]
	v_mov_b64_e32 v[8:9], v[108:109]
	v_mov_b64_e32 v[12:13], v[92:93]
	v_mov_b64_e32 v[24:25], v[96:97]
	v_mov_b64_e32 v[36:37], v[80:81]
	v_mov_b64_e32 v[48:49], v[84:85]
	v_mov_b64_e32 v[52:53], v[64:65]
	v_mov_b64_e32 v[70:71], v[66:67]
	v_mov_b64_e32 v[74:75], v[54:55]
	v_mov_b64_e32 v[86:87], v[58:59]
	v_mov_b64_e32 v[98:99], v[38:39]
	v_mov_b64_e32 v[110:111], v[42:43]
	v_mov_b64_e32 v[114:115], v[26:27]
	v_mov_b64_e32 v[118:119], v[30:31]
	v_mov_b64_e32 v[122:123], v[14:15]
	v_mov_b64_e32 v[126:127], v[18:19]
	s_mov_b32 s8, s10
	s_cbranch_vccz .LBB0_121
.LBB0_119:
	s_barrier
	s_add_i32 s10, s8, s2
	s_cmpk_gt_i32 s10, 0x7fff
	s_cselect_b64 s[6:7], -1, 0
	s_and_b64 vcc, exec, s[6:7]
	s_cbranch_vccnz .LBB0_118
	s_mov_b32 s100, s10
	s_and_b32 s101, s100, 7
	s_lshl_b32 s101, s101, 5
	s_bfe_u32 s10, s100, 0x30005
	s_or_b32 s10, s10, s101
	s_andn2_b32 s101, s100, 0xe7
	s_or_b32 s10, s10, s101
	s_ashr_i32 s9, s10, 31
	s_lshr_b32 s9, s9, 24
	s_add_i32 s9, s10, s9
	s_ashr_i32 s12, s9, 8
	s_ashr_i32 s13, s12, 31
	s_lshl_b64 s[12:13], s[12:13], 22
	s_add_u32 s11, s4, s12
	s_addc_u32 s14, s5, s13
	s_and_b32 s9, s9, 0xffffff00
	s_sub_i32 s9, s10, s9
	s_mov_b32 s10, s100
	s_ashr_i32 s12, s9, 31
	s_lshr_b32 s12, s12, 27
	s_add_i32 s12, s9, s12
	s_and_b32 s13, s12, 0x7ffffe0
	s_sub_i32 s9, s9, s13
	s_lshl_b32 s12, s12, 2
	s_and_b32 s13, s12, 0xffffff80
	s_lshl_b32 s12, s9, 5
	v_or_b32_e32 v102, s13, v1
	s_ashr_i32 s13, s12, 31
	s_lshl_b64 s[12:13], s[12:13], 2
	s_add_u32 s12, s11, s12
	s_addc_u32 s13, s14, s13
	v_ashrrev_i32_e32 v103, 31, v102
	v_lshl_add_u64 v[104:105], s[12:13], 0, v[136:137]
	v_lshlrev_b64 v[14:15], 12, v[102:103]
	v_lshl_add_u64 v[26:27], v[104:105], 0, v[14:15]
	v_or_b32_e32 v14, 8, v102
	v_ashrrev_i32_e32 v15, 31, v14
	v_lshlrev_b64 v[14:15], 12, v[14:15]
	v_lshl_add_u64 v[28:29], v[104:105], 0, v[14:15]
	global_load_dwordx4 v[18:21], v[26:27], off nt
	global_load_dwordx4 v[14:17], v[28:29], off nt
	v_or_b32_e32 v26, 16, v102
	v_ashrrev_i32_e32 v27, 31, v26
	v_lshlrev_b64 v[26:27], 12, v[26:27]
	v_lshl_add_u64 v[38:39], v[104:105], 0, v[26:27]
	v_or_b32_e32 v26, 24, v102
	v_ashrrev_i32_e32 v27, 31, v26
	v_lshlrev_b64 v[26:27], 12, v[26:27]
	v_lshl_add_u64 v[40:41], v[104:105], 0, v[26:27]
	global_load_dwordx4 v[30:33], v[38:39], off nt
	global_load_dwordx4 v[26:29], v[40:41], off nt
	v_or_b32_e32 v38, 32, v102
	v_ashrrev_i32_e32 v39, 31, v38
	v_lshlrev_b64 v[38:39], 12, v[38:39]
	v_lshl_add_u64 v[54:55], v[104:105], 0, v[38:39]
	v_or_b32_e32 v38, 40, v102
	v_ashrrev_i32_e32 v39, 31, v38
	v_lshlrev_b64 v[38:39], 12, v[38:39]
	v_lshl_add_u64 v[56:57], v[104:105], 0, v[38:39]
	global_load_dwordx4 v[42:45], v[54:55], off nt
	global_load_dwordx4 v[38:41], v[56:57], off nt
	v_or_b32_e32 v54, 48, v102
	v_ashrrev_i32_e32 v55, 31, v54
	v_lshlrev_b64 v[54:55], 12, v[54:55]
	v_lshl_add_u64 v[62:63], v[104:105], 0, v[54:55]
	v_or_b32_e32 v54, 56, v102
	v_ashrrev_i32_e32 v55, 31, v54
	v_lshlrev_b64 v[54:55], 12, v[54:55]
	v_lshl_add_u64 v[64:65], v[104:105], 0, v[54:55]
	global_load_dwordx4 v[58:61], v[62:63], off nt
	global_load_dwordx4 v[54:57], v[64:65], off nt
	v_or_b32_e32 v62, 64, v102
	v_ashrrev_i32_e32 v63, 31, v62
	v_lshlrev_b64 v[62:63], 12, v[62:63]
	v_lshl_add_u64 v[78:79], v[104:105], 0, v[62:63]
	v_or_b32_e32 v62, 0x48, v102
	v_ashrrev_i32_e32 v63, 31, v62
	v_lshlrev_b64 v[62:63], 12, v[62:63]
	v_lshl_add_u64 v[80:81], v[104:105], 0, v[62:63]
	global_load_dwordx4 v[66:69], v[78:79], off nt
	global_load_dwordx4 v[62:65], v[80:81], off nt
	v_or_b32_e32 v78, 0x50, v102
	v_or_b32_e32 v80, 0x58, v102
	v_or_b32_e32 v90, 0x60, v102
	v_or_b32_e32 v92, 0x68, v102
	v_or_b32_e32 v106, 0x70, v102
	v_or_b32_e32 v102, 0x78, v102
	v_ashrrev_i32_e32 v79, 31, v78
	v_ashrrev_i32_e32 v81, 31, v80
	v_ashrrev_i32_e32 v91, 31, v90
	v_ashrrev_i32_e32 v93, 31, v92
	v_ashrrev_i32_e32 v107, 31, v106
	v_ashrrev_i32_e32 v103, 31, v102
	v_lshlrev_b64 v[78:79], 12, v[78:79]
	v_lshlrev_b64 v[80:81], 12, v[80:81]
	v_lshlrev_b64 v[90:91], 12, v[90:91]
	v_lshlrev_b64 v[92:93], 12, v[92:93]
	v_lshlrev_b64 v[106:107], 12, v[106:107]
	v_lshlrev_b64 v[102:103], 12, v[102:103]
	v_lshl_add_u64 v[78:79], v[104:105], 0, v[78:79]
	v_lshl_add_u64 v[80:81], v[104:105], 0, v[80:81]
	v_lshl_add_u64 v[90:91], v[104:105], 0, v[90:91]
	v_lshl_add_u64 v[92:93], v[104:105], 0, v[92:93]
	v_lshl_add_u64 v[106:107], v[104:105], 0, v[106:107]
	v_lshl_add_u64 v[102:103], v[104:105], 0, v[102:103]
	global_load_dwordx4 v[82:85], v[78:79], off nt
	s_nop 0
	global_load_dwordx4 v[78:81], v[80:81], off nt
	s_nop 0
	global_load_dwordx4 v[94:97], v[90:91], off nt
	s_nop 0
	global_load_dwordx4 v[90:93], v[92:93], off nt
	s_nop 0
	global_load_dwordx4 v[106:109], v[106:107], off nt
	s_nop 0
	global_load_dwordx4 v[102:105], v[102:103], off nt
	s_branch .LBB0_118

	.amdhsa_kernel _Z9trunk_fwd4Args
		.amdhsa_group_segment_fixed_size 0
		.amdhsa_private_segment_fixed_size 0
		.amdhsa_kernarg_size 472
		.amdhsa_user_sgpr_count 2
		.amdhsa_user_sgpr_dispatch_ptr 0
		.amdhsa_user_sgpr_queue_ptr 0
		.amdhsa_user_sgpr_kernarg_segment_ptr 1
		.amdhsa_user_sgpr_dispatch_id 0
		.amdhsa_user_sgpr_kernarg_preload_length 0
		.amdhsa_user_sgpr_kernarg_preload_offset 0
		.amdhsa_user_sgpr_private_segment_size 0
		.amdhsa_uses_dynamic_stack 0
		.amdhsa_enable_private_segment 0
		.amdhsa_system_sgpr_workgroup_id_x 1
		.amdhsa_system_sgpr_workgroup_id_y 0
		.amdhsa_system_sgpr_workgroup_id_z 0
		.amdhsa_system_sgpr_workgroup_info 0
		.amdhsa_system_vgpr_workitem_id 0
		.amdhsa_next_free_vgpr 256
		.amdhsa_next_free_sgpr 102
		.amdhsa_accum_offset 256
		.amdhsa_reserve_vcc 1
		.amdhsa_float_round_mode_32 0
		.amdhsa_float_round_mode_16_64 0
		.amdhsa_float_denorm_mode_32 3
		.amdhsa_float_denorm_mode_16_64 3
		.amdhsa_dx10_clamp 1
		.amdhsa_ieee_mode 1
		.amdhsa_fp16_overflow 0
		.amdhsa_tg_split 0
		.amdhsa_exception_fp_ieee_invalid_op 0
		.amdhsa_exception_fp_denorm_src 0
		.amdhsa_exception_fp_ieee_div_zero 0
		.amdhsa_exception_fp_ieee_overflow 0
		.amdhsa_exception_fp_ieee_underflow 0
		.amdhsa_exception_fp_ieee_inexact 0
		.amdhsa_exception_int_div_zero 0
	.end_amdhsa_kernel

amdhsa.kernels:
  - .agpr_count:     0
    .args:
      - .offset:         0
        .size:           216
        .value_kind:     by_value
      - .offset:         216
        .size:           4
        .value_kind:     hidden_block_count_x
      - .offset:         220
        .size:           4
        .value_kind:     hidden_block_count_y
      - .offset:         224
        .size:           4
        .value_kind:     hidden_block_count_z
      - .offset:         228
        .size:           2
        .value_kind:     hidden_group_size_x
      - .offset:         230
        .size:           2
        .value_kind:     hidden_group_size_y
      - .offset:         232
        .size:           2
        .value_kind:     hidden_group_size_z
      - .offset:         234
        .size:           2
        .value_kind:     hidden_remainder_x
      - .offset:         236
        .size:           2
        .value_kind:     hidden_remainder_y
      - .offset:         238
        .size:           2
        .value_kind:     hidden_remainder_z
      - .offset:         256
        .size:           8
        .value_kind:     hidden_global_offset_x
      - .offset:         264
        .size:           8
        .value_kind:     hidden_global_offset_y
      - .offset:         272
        .size:           8
        .value_kind:     hidden_global_offset_z
      - .offset:         280
        .size:           2
        .value_kind:     hidden_grid_dims
      - .offset:         336
        .size:           4
        .value_kind:     hidden_dynamic_lds_size
    .group_segment_fixed_size: 0
    .kernarg_segment_align: 8
    .kernarg_segment_size: 472
    .language:       OpenCL C
    .language_version:
      - 2
      - 0
    .max_flat_workgroup_size: 512
    .name:           _Z9trunk_fwd4Args
    .private_segment_fixed_size: 0
    .sgpr_count:     108
    .sgpr_spill_count: 137
    .symbol:         _Z9trunk_fwd4Args.kd
    .uniform_work_group_size: 1
    .uses_dynamic_stack: false
    .vgpr_count:     256
    .vgpr_spill_count: 0
    .wavefront_size: 64
